# attention block epilogues: non-temporal output stores (keep the K/V tiles in L2)
# speedup vs baseline: 1.0239x; 1.0239x over previous
.LBB0_635:
	s_waitcnt vmcnt(8)
	s_waitcnt vmcnt(9)
	ds_write_b128 v221, v[98:101] offset:32768
	s_waitcnt vmcnt(8)
	ds_write_b128 v221, v[102:105] offset:40960
	s_and_saveexec_b64 s[8:9], s[4:5]
	ds_write_b32 v223, v114
	s_or_b64 exec, exec, s[8:9]
	s_waitcnt lgkmcnt(0)
	ds_read_b128 v[66:69], v205
	ds_read_b128 v[70:73], v205 offset:32
	ds_read_b128 v[74:77], v205 offset:64
	ds_read_b128 v[78:81], v205 offset:96
	s_add_u32 s0, s22, s24
	s_addc_u32 s1, s23, s25
	s_lshl_b32 s2, s43, 12
	s_add_u32 s0, s0, s2
	s_addc_u32 s1, s1, 0
	v_lshrrev_b32_e32 v82, 6, v254
	v_lshlrev_b32_e32 v82, 13, v82
	v_add_u32_e32 v82, 0x11000, v82
	v_and_b32_e32 v83, 31, v213
	v_lshrrev_b32_e32 v84, 5, v213
	v_lshlrev_b32_e32 v83, 1, v83
	v_lshl_add_u32 v83, v84, 10, v83
	v_add_u32_e32 v83, v82, v83
	v_lshl_add_u32 v82, v213, 4, v82
	v_lshrrev_b32_e32 v84, 4, v213
	v_and_b32_e32 v85, 15, v213
	v_lshlrev_b32_e32 v85, 4, v85
	v_lshl_add_u32 v84, v84, 12, v85
	s_waitcnt lgkmcnt(0)
	v_rcp_f32_e32 v66, v66
	v_rcp_f32_e32 v67, v67
	v_rcp_f32_e32 v68, v68
	v_rcp_f32_e32 v69, v69
	v_rcp_f32_e32 v70, v70
	v_rcp_f32_e32 v71, v71
	v_rcp_f32_e32 v72, v72
	v_rcp_f32_e32 v73, v73
	v_rcp_f32_e32 v74, v74
	v_rcp_f32_e32 v75, v75
	v_rcp_f32_e32 v76, v76
	v_rcp_f32_e32 v77, v77
	v_rcp_f32_e32 v78, v78
	v_rcp_f32_e32 v79, v79
	v_rcp_f32_e32 v80, v80
	v_rcp_f32_e32 v81, v81
	v_mul_f32_e32 v50, v50, v66
	v_mul_f32_e32 v34, v34, v66
	v_mul_f32_e32 v18, v18, v66
	v_mul_f32_e32 v2, v2, v66
	v_mul_f32_e32 v51, v51, v67
	v_mul_f32_e32 v35, v35, v67
	v_mul_f32_e32 v19, v19, v67
	v_mul_f32_e32 v3, v3, v67
	v_mov_b32_dpp v114, v50 quad_perm:[1,0,3,2] row_mask:0xf bank_mask:0xf
	v_mov_b32_dpp v115, v34 quad_perm:[1,0,3,2] row_mask:0xf bank_mask:0xf
	v_mov_b32_dpp v116, v18 quad_perm:[1,0,3,2] row_mask:0xf bank_mask:0xf
	v_mov_b32_dpp v117, v2 quad_perm:[1,0,3,2] row_mask:0xf bank_mask:0xf
	v_mov_b32_dpp v118, v51 quad_perm:[1,0,3,2] row_mask:0xf bank_mask:0xf
	v_mov_b32_dpp v119, v35 quad_perm:[1,0,3,2] row_mask:0xf bank_mask:0xf
	v_mov_b32_dpp v120, v19 quad_perm:[1,0,3,2] row_mask:0xf bank_mask:0xf
	v_mov_b32_dpp v121, v3 quad_perm:[1,0,3,2] row_mask:0xf bank_mask:0xf
	v_cvt_pk_bf16_f32 v50, v50, v114
	v_cvt_pk_bf16_f32 v34, v34, v115
	v_cvt_pk_bf16_f32 v18, v18, v116
	v_cvt_pk_bf16_f32 v2, v2, v117
	v_cvt_pk_bf16_f32 v51, v51, v118
	v_cvt_pk_bf16_f32 v35, v35, v119
	v_cvt_pk_bf16_f32 v19, v19, v120
	v_cvt_pk_bf16_f32 v3, v3, v121
	v_mul_f32_e32 v52, v52, v68
	v_mul_f32_e32 v36, v36, v68
	v_mul_f32_e32 v20, v20, v68
	v_mul_f32_e32 v4, v4, v68
	v_mul_f32_e32 v53, v53, v69
	v_mul_f32_e32 v37, v37, v69
	v_mul_f32_e32 v21, v21, v69
	v_mul_f32_e32 v5, v5, v69
	v_mov_b32_dpp v114, v52 quad_perm:[1,0,3,2] row_mask:0xf bank_mask:0xf
	v_mov_b32_dpp v115, v36 quad_perm:[1,0,3,2] row_mask:0xf bank_mask:0xf
	v_mov_b32_dpp v116, v20 quad_perm:[1,0,3,2] row_mask:0xf bank_mask:0xf
	v_mov_b32_dpp v117, v4 quad_perm:[1,0,3,2] row_mask:0xf bank_mask:0xf
	v_mov_b32_dpp v118, v53 quad_perm:[1,0,3,2] row_mask:0xf bank_mask:0xf
	v_mov_b32_dpp v119, v37 quad_perm:[1,0,3,2] row_mask:0xf bank_mask:0xf
	v_mov_b32_dpp v120, v21 quad_perm:[1,0,3,2] row_mask:0xf bank_mask:0xf
	v_mov_b32_dpp v121, v5 quad_perm:[1,0,3,2] row_mask:0xf bank_mask:0xf
	v_cvt_pk_bf16_f32 v52, v52, v114
	v_cvt_pk_bf16_f32 v36, v36, v115
	v_cvt_pk_bf16_f32 v20, v20, v116
	v_cvt_pk_bf16_f32 v4, v4, v117
	v_cvt_pk_bf16_f32 v53, v53, v118
	v_cvt_pk_bf16_f32 v37, v37, v119
	v_cvt_pk_bf16_f32 v21, v21, v120
	v_cvt_pk_bf16_f32 v5, v5, v121
	v_mul_f32_e32 v54, v54, v70
	v_mul_f32_e32 v38, v38, v70
	v_mul_f32_e32 v22, v22, v70
	v_mul_f32_e32 v6, v6, v70
	v_mul_f32_e32 v55, v55, v71
	v_mul_f32_e32 v39, v39, v71
	v_mul_f32_e32 v23, v23, v71
	v_mul_f32_e32 v7, v7, v71
	v_mov_b32_dpp v114, v54 quad_perm:[1,0,3,2] row_mask:0xf bank_mask:0xf
	v_mov_b32_dpp v115, v38 quad_perm:[1,0,3,2] row_mask:0xf bank_mask:0xf
	v_mov_b32_dpp v116, v22 quad_perm:[1,0,3,2] row_mask:0xf bank_mask:0xf
	v_mov_b32_dpp v117, v6 quad_perm:[1,0,3,2] row_mask:0xf bank_mask:0xf
	v_mov_b32_dpp v118, v55 quad_perm:[1,0,3,2] row_mask:0xf bank_mask:0xf
	v_mov_b32_dpp v119, v39 quad_perm:[1,0,3,2] row_mask:0xf bank_mask:0xf
	v_mov_b32_dpp v120, v23 quad_perm:[1,0,3,2] row_mask:0xf bank_mask:0xf
	v_mov_b32_dpp v121, v7 quad_perm:[1,0,3,2] row_mask:0xf bank_mask:0xf
	v_cvt_pk_bf16_f32 v54, v54, v114
	v_cvt_pk_bf16_f32 v38, v38, v115
	v_cvt_pk_bf16_f32 v22, v22, v116
	v_cvt_pk_bf16_f32 v6, v6, v117
	v_cvt_pk_bf16_f32 v55, v55, v118
	v_cvt_pk_bf16_f32 v39, v39, v119
	v_cvt_pk_bf16_f32 v23, v23, v120
	v_cvt_pk_bf16_f32 v7, v7, v121
	v_mul_f32_e32 v56, v56, v72
	v_mul_f32_e32 v40, v40, v72
	v_mul_f32_e32 v24, v24, v72
	v_mul_f32_e32 v8, v8, v72
	v_mul_f32_e32 v57, v57, v73
	v_mul_f32_e32 v41, v41, v73
	v_mul_f32_e32 v25, v25, v73
	v_mul_f32_e32 v9, v9, v73
	v_mov_b32_dpp v114, v56 quad_perm:[1,0,3,2] row_mask:0xf bank_mask:0xf
	v_mov_b32_dpp v115, v40 quad_perm:[1,0,3,2] row_mask:0xf bank_mask:0xf
	v_mov_b32_dpp v116, v24 quad_perm:[1,0,3,2] row_mask:0xf bank_mask:0xf
	v_mov_b32_dpp v117, v8 quad_perm:[1,0,3,2] row_mask:0xf bank_mask:0xf
	v_mov_b32_dpp v118, v57 quad_perm:[1,0,3,2] row_mask:0xf bank_mask:0xf
	v_mov_b32_dpp v119, v41 quad_perm:[1,0,3,2] row_mask:0xf bank_mask:0xf
	v_mov_b32_dpp v120, v25 quad_perm:[1,0,3,2] row_mask:0xf bank_mask:0xf
	v_mov_b32_dpp v121, v9 quad_perm:[1,0,3,2] row_mask:0xf bank_mask:0xf
	v_cvt_pk_bf16_f32 v56, v56, v114
	v_cvt_pk_bf16_f32 v40, v40, v115
	v_cvt_pk_bf16_f32 v24, v24, v116
	v_cvt_pk_bf16_f32 v8, v8, v117
	v_cvt_pk_bf16_f32 v57, v57, v118
	v_cvt_pk_bf16_f32 v41, v41, v119
	v_cvt_pk_bf16_f32 v25, v25, v120
	v_cvt_pk_bf16_f32 v9, v9, v121
	v_mul_f32_e32 v58, v58, v74
	v_mul_f32_e32 v42, v42, v74
	v_mul_f32_e32 v26, v26, v74
	v_mul_f32_e32 v10, v10, v74
	v_mul_f32_e32 v59, v59, v75
	v_mul_f32_e32 v43, v43, v75
	v_mul_f32_e32 v27, v27, v75
	v_mul_f32_e32 v11, v11, v75
	v_mov_b32_dpp v114, v58 quad_perm:[1,0,3,2] row_mask:0xf bank_mask:0xf
	v_mov_b32_dpp v115, v42 quad_perm:[1,0,3,2] row_mask:0xf bank_mask:0xf
	v_mov_b32_dpp v116, v26 quad_perm:[1,0,3,2] row_mask:0xf bank_mask:0xf
	v_mov_b32_dpp v117, v10 quad_perm:[1,0,3,2] row_mask:0xf bank_mask:0xf
	v_mov_b32_dpp v118, v59 quad_perm:[1,0,3,2] row_mask:0xf bank_mask:0xf
	v_mov_b32_dpp v119, v43 quad_perm:[1,0,3,2] row_mask:0xf bank_mask:0xf
	v_mov_b32_dpp v120, v27 quad_perm:[1,0,3,2] row_mask:0xf bank_mask:0xf
	v_mov_b32_dpp v121, v11 quad_perm:[1,0,3,2] row_mask:0xf bank_mask:0xf
	v_cvt_pk_bf16_f32 v58, v58, v114
	v_cvt_pk_bf16_f32 v42, v42, v115
	v_cvt_pk_bf16_f32 v26, v26, v116
	v_cvt_pk_bf16_f32 v10, v10, v117
	v_cvt_pk_bf16_f32 v59, v59, v118
	v_cvt_pk_bf16_f32 v43, v43, v119
	v_cvt_pk_bf16_f32 v27, v27, v120
	v_cvt_pk_bf16_f32 v11, v11, v121
	v_mul_f32_e32 v60, v60, v76
	v_mul_f32_e32 v44, v44, v76
	v_mul_f32_e32 v28, v28, v76
	v_mul_f32_e32 v12, v12, v76
	v_mul_f32_e32 v61, v61, v77
	v_mul_f32_e32 v45, v45, v77
	v_mul_f32_e32 v29, v29, v77
	v_mul_f32_e32 v13, v13, v77
	v_mov_b32_dpp v114, v60 quad_perm:[1,0,3,2] row_mask:0xf bank_mask:0xf
	v_mov_b32_dpp v115, v44 quad_perm:[1,0,3,2] row_mask:0xf bank_mask:0xf
	v_mov_b32_dpp v116, v28 quad_perm:[1,0,3,2] row_mask:0xf bank_mask:0xf
	v_mov_b32_dpp v117, v12 quad_perm:[1,0,3,2] row_mask:0xf bank_mask:0xf
	v_mov_b32_dpp v118, v61 quad_perm:[1,0,3,2] row_mask:0xf bank_mask:0xf
	v_mov_b32_dpp v119, v45 quad_perm:[1,0,3,2] row_mask:0xf bank_mask:0xf
	v_mov_b32_dpp v120, v29 quad_perm:[1,0,3,2] row_mask:0xf bank_mask:0xf
	v_mov_b32_dpp v121, v13 quad_perm:[1,0,3,2] row_mask:0xf bank_mask:0xf
	v_cvt_pk_bf16_f32 v60, v60, v114
	v_cvt_pk_bf16_f32 v44, v44, v115
	v_cvt_pk_bf16_f32 v28, v28, v116
	v_cvt_pk_bf16_f32 v12, v12, v117
	v_cvt_pk_bf16_f32 v61, v61, v118
	v_cvt_pk_bf16_f32 v45, v45, v119
	v_cvt_pk_bf16_f32 v29, v29, v120
	v_cvt_pk_bf16_f32 v13, v13, v121
	v_mul_f32_e32 v62, v62, v78
	v_mul_f32_e32 v46, v46, v78
	v_mul_f32_e32 v30, v30, v78
	v_mul_f32_e32 v14, v14, v78
	v_mul_f32_e32 v63, v63, v79
	v_mul_f32_e32 v47, v47, v79
	v_mul_f32_e32 v31, v31, v79
	v_mul_f32_e32 v15, v15, v79
	v_mov_b32_dpp v114, v62 quad_perm:[1,0,3,2] row_mask:0xf bank_mask:0xf
	v_mov_b32_dpp v115, v46 quad_perm:[1,0,3,2] row_mask:0xf bank_mask:0xf
	v_mov_b32_dpp v116, v30 quad_perm:[1,0,3,2] row_mask:0xf bank_mask:0xf
	v_mov_b32_dpp v117, v14 quad_perm:[1,0,3,2] row_mask:0xf bank_mask:0xf
	v_mov_b32_dpp v118, v63 quad_perm:[1,0,3,2] row_mask:0xf bank_mask:0xf
	v_mov_b32_dpp v119, v47 quad_perm:[1,0,3,2] row_mask:0xf bank_mask:0xf
	v_mov_b32_dpp v120, v31 quad_perm:[1,0,3,2] row_mask:0xf bank_mask:0xf
	v_mov_b32_dpp v121, v15 quad_perm:[1,0,3,2] row_mask:0xf bank_mask:0xf
	v_cvt_pk_bf16_f32 v62, v62, v114
	v_cvt_pk_bf16_f32 v46, v46, v115
	v_cvt_pk_bf16_f32 v30, v30, v116
	v_cvt_pk_bf16_f32 v14, v14, v117
	v_cvt_pk_bf16_f32 v63, v63, v118
	v_cvt_pk_bf16_f32 v47, v47, v119
	v_cvt_pk_bf16_f32 v31, v31, v120
	v_cvt_pk_bf16_f32 v15, v15, v121
	v_mul_f32_e32 v64, v64, v80
	v_mul_f32_e32 v48, v48, v80
	v_mul_f32_e32 v32, v32, v80
	v_mul_f32_e32 v16, v16, v80
	v_mul_f32_e32 v65, v65, v81
	v_mul_f32_e32 v49, v49, v81
	v_mul_f32_e32 v33, v33, v81
	v_mul_f32_e32 v17, v17, v81
	v_mov_b32_dpp v114, v64 quad_perm:[1,0,3,2] row_mask:0xf bank_mask:0xf
	v_mov_b32_dpp v115, v48 quad_perm:[1,0,3,2] row_mask:0xf bank_mask:0xf
	v_mov_b32_dpp v116, v32 quad_perm:[1,0,3,2] row_mask:0xf bank_mask:0xf
	v_mov_b32_dpp v117, v16 quad_perm:[1,0,3,2] row_mask:0xf bank_mask:0xf
	v_mov_b32_dpp v118, v65 quad_perm:[1,0,3,2] row_mask:0xf bank_mask:0xf
	v_mov_b32_dpp v119, v49 quad_perm:[1,0,3,2] row_mask:0xf bank_mask:0xf
	v_mov_b32_dpp v120, v33 quad_perm:[1,0,3,2] row_mask:0xf bank_mask:0xf
	v_mov_b32_dpp v121, v17 quad_perm:[1,0,3,2] row_mask:0xf bank_mask:0xf
	v_cvt_pk_bf16_f32 v64, v64, v114
	v_cvt_pk_bf16_f32 v48, v48, v115
	v_cvt_pk_bf16_f32 v32, v32, v116
	v_cvt_pk_bf16_f32 v16, v16, v117
	v_cvt_pk_bf16_f32 v65, v65, v118
	v_cvt_pk_bf16_f32 v49, v49, v119
	v_cvt_pk_bf16_f32 v33, v33, v120
	v_cvt_pk_bf16_f32 v17, v17, v121
	s_mov_b64 s[100:101], exec
	s_and_b64 exec, exec, s[6:7]
	ds_write_b32 v83, v50
	ds_write_b32 v83, v34 offset:64
	ds_write_b32 v83, v18 offset:128
	ds_write_b32 v83, v2 offset:192
	ds_write_b32 v83, v51 offset:256
	ds_write_b32 v83, v35 offset:320
	ds_write_b32 v83, v19 offset:384
	ds_write_b32 v83, v3 offset:448
	ds_write_b32 v83, v52 offset:512
	ds_write_b32 v83, v36 offset:576
	ds_write_b32 v83, v20 offset:640
	ds_write_b32 v83, v4 offset:704
	ds_write_b32 v83, v53 offset:768
	ds_write_b32 v83, v37 offset:832
	ds_write_b32 v83, v21 offset:896
	ds_write_b32 v83, v5 offset:960
	ds_write_b32 v83, v54 offset:2048
	ds_write_b32 v83, v38 offset:2112
	ds_write_b32 v83, v22 offset:2176
	ds_write_b32 v83, v6 offset:2240
	ds_write_b32 v83, v55 offset:2304
	ds_write_b32 v83, v39 offset:2368
	ds_write_b32 v83, v23 offset:2432
	ds_write_b32 v83, v7 offset:2496
	ds_write_b32 v83, v56 offset:2560
	ds_write_b32 v83, v40 offset:2624
	ds_write_b32 v83, v24 offset:2688
	ds_write_b32 v83, v8 offset:2752
	ds_write_b32 v83, v57 offset:2816
	ds_write_b32 v83, v41 offset:2880
	ds_write_b32 v83, v25 offset:2944
	ds_write_b32 v83, v9 offset:3008
	ds_write_b32 v83, v58 offset:4096
	ds_write_b32 v83, v42 offset:4160
	ds_write_b32 v83, v26 offset:4224
	ds_write_b32 v83, v10 offset:4288
	ds_write_b32 v83, v59 offset:4352
	ds_write_b32 v83, v43 offset:4416
	ds_write_b32 v83, v27 offset:4480
	ds_write_b32 v83, v11 offset:4544
	ds_write_b32 v83, v60 offset:4608
	ds_write_b32 v83, v44 offset:4672
	ds_write_b32 v83, v28 offset:4736
	ds_write_b32 v83, v12 offset:4800
	ds_write_b32 v83, v61 offset:4864
	ds_write_b32 v83, v45 offset:4928
	ds_write_b32 v83, v29 offset:4992
	ds_write_b32 v83, v13 offset:5056
	ds_write_b32 v83, v62 offset:6144
	ds_write_b32 v83, v46 offset:6208
	ds_write_b32 v83, v30 offset:6272
	ds_write_b32 v83, v14 offset:6336
	ds_write_b32 v83, v63 offset:6400
	ds_write_b32 v83, v47 offset:6464
	ds_write_b32 v83, v31 offset:6528
	ds_write_b32 v83, v15 offset:6592
	ds_write_b32 v83, v64 offset:6656
	ds_write_b32 v83, v48 offset:6720
	ds_write_b32 v83, v32 offset:6784
	ds_write_b32 v83, v16 offset:6848
	ds_write_b32 v83, v65 offset:6912
	ds_write_b32 v83, v49 offset:6976
	ds_write_b32 v83, v33 offset:7040
	ds_write_b32 v83, v17 offset:7104
	s_mov_b64 exec, s[100:101]
	ds_read_b128 v[66:69], v82
	ds_read_b128 v[70:73], v82 offset:1024
	ds_read_b128 v[74:77], v82 offset:2048
	ds_read_b128 v[78:81], v82 offset:3072
	ds_read_b128 v[86:89], v82 offset:4096
	ds_read_b128 v[90:93], v82 offset:5120
	ds_read_b128 v[94:97], v82 offset:6144
	ds_read_b128 v[98:101], v82 offset:7168
	s_waitcnt lgkmcnt(7)
	global_store_dwordx4 v84, v[66:69], s[0:1] nt
	s_waitcnt lgkmcnt(6)
	v_add_u32_e32 v85, 16384, v84
	global_store_dwordx4 v85, v[70:73], s[0:1] nt
	s_waitcnt lgkmcnt(5)
	v_add_u32_e32 v85, 32768, v84
	global_store_dwordx4 v85, v[74:77], s[0:1] nt
	s_waitcnt lgkmcnt(4)
	v_add_u32_e32 v85, 49152, v84
	global_store_dwordx4 v85, v[78:81], s[0:1] nt
	s_waitcnt lgkmcnt(3)
	v_add_u32_e32 v85, 65536, v84
	global_store_dwordx4 v85, v[86:89], s[0:1] nt
	s_waitcnt lgkmcnt(2)
	v_add_u32_e32 v85, 81920, v84
	global_store_dwordx4 v85, v[90:93], s[0:1] nt
	s_waitcnt lgkmcnt(1)
	v_add_u32_e32 v85, 98304, v84
	global_store_dwordx4 v85, v[94:97], s[0:1] nt
	s_waitcnt lgkmcnt(0)
	v_add_u32_e32 v85, 114688, v84
	global_store_dwordx4 v85, v[98:101], s[0:1] nt
	s_branch .LBB0_593

.LBB0_862:
	s_waitcnt vmcnt(8)
	s_waitcnt vmcnt(9)
	ds_write_b128 v222, v[98:101] offset:32768
	s_waitcnt vmcnt(8)
	ds_write_b128 v222, v[102:105] offset:40960
	s_and_saveexec_b64 s[8:9], s[4:5]
	ds_write_b32 v224, v114
	s_or_b64 exec, exec, s[8:9]
	s_waitcnt lgkmcnt(0)
	ds_read_b128 v[66:69], v205
	ds_read_b128 v[70:73], v205 offset:32
	ds_read_b128 v[74:77], v205 offset:64
	ds_read_b128 v[78:81], v205 offset:96
	s_add_u32 s0, s26, s28
	s_addc_u32 s1, s27, s29
	s_lshl_b32 s2, s47, 12
	s_add_u32 s0, s0, s2
	s_addc_u32 s1, s1, 0
	v_lshrrev_b32_e32 v82, 6, v254
	v_lshlrev_b32_e32 v82, 13, v82
	v_add_u32_e32 v82, 0x11000, v82
	v_and_b32_e32 v83, 31, v214
	v_lshrrev_b32_e32 v84, 5, v214
	v_lshlrev_b32_e32 v83, 1, v83
	v_lshl_add_u32 v83, v84, 10, v83
	v_add_u32_e32 v83, v82, v83
	v_lshl_add_u32 v82, v214, 4, v82
	v_lshrrev_b32_e32 v84, 4, v214
	v_and_b32_e32 v85, 15, v214
	v_lshlrev_b32_e32 v85, 4, v85
	v_lshl_add_u32 v84, v84, 12, v85
	s_waitcnt lgkmcnt(0)
	v_rcp_f32_e32 v66, v66
	v_rcp_f32_e32 v67, v67
	v_rcp_f32_e32 v68, v68
	v_rcp_f32_e32 v69, v69
	v_rcp_f32_e32 v70, v70
	v_rcp_f32_e32 v71, v71
	v_rcp_f32_e32 v72, v72
	v_rcp_f32_e32 v73, v73
	v_rcp_f32_e32 v74, v74
	v_rcp_f32_e32 v75, v75
	v_rcp_f32_e32 v76, v76
	v_rcp_f32_e32 v77, v77
	v_rcp_f32_e32 v78, v78
	v_rcp_f32_e32 v79, v79
	v_rcp_f32_e32 v80, v80
	v_rcp_f32_e32 v81, v81
	v_mul_f32_e32 v50, v50, v66
	v_mul_f32_e32 v34, v34, v66
	v_mul_f32_e32 v18, v18, v66
	v_mul_f32_e32 v2, v2, v66
	v_mul_f32_e32 v51, v51, v67
	v_mul_f32_e32 v35, v35, v67
	v_mul_f32_e32 v19, v19, v67
	v_mul_f32_e32 v3, v3, v67
	v_mov_b32_dpp v114, v50 quad_perm:[1,0,3,2] row_mask:0xf bank_mask:0xf
	v_mov_b32_dpp v115, v34 quad_perm:[1,0,3,2] row_mask:0xf bank_mask:0xf
	v_mov_b32_dpp v116, v18 quad_perm:[1,0,3,2] row_mask:0xf bank_mask:0xf
	v_mov_b32_dpp v117, v2 quad_perm:[1,0,3,2] row_mask:0xf bank_mask:0xf
	v_mov_b32_dpp v118, v51 quad_perm:[1,0,3,2] row_mask:0xf bank_mask:0xf
	v_mov_b32_dpp v119, v35 quad_perm:[1,0,3,2] row_mask:0xf bank_mask:0xf
	v_mov_b32_dpp v120, v19 quad_perm:[1,0,3,2] row_mask:0xf bank_mask:0xf
	v_mov_b32_dpp v121, v3 quad_perm:[1,0,3,2] row_mask:0xf bank_mask:0xf
	v_cvt_pk_bf16_f32 v50, v50, v114
	v_cvt_pk_bf16_f32 v34, v34, v115
	v_cvt_pk_bf16_f32 v18, v18, v116
	v_cvt_pk_bf16_f32 v2, v2, v117
	v_cvt_pk_bf16_f32 v51, v51, v118
	v_cvt_pk_bf16_f32 v35, v35, v119
	v_cvt_pk_bf16_f32 v19, v19, v120
	v_cvt_pk_bf16_f32 v3, v3, v121
	v_mul_f32_e32 v52, v52, v68
	v_mul_f32_e32 v36, v36, v68
	v_mul_f32_e32 v20, v20, v68
	v_mul_f32_e32 v4, v4, v68
	v_mul_f32_e32 v53, v53, v69
	v_mul_f32_e32 v37, v37, v69
	v_mul_f32_e32 v21, v21, v69
	v_mul_f32_e32 v5, v5, v69
	v_mov_b32_dpp v114, v52 quad_perm:[1,0,3,2] row_mask:0xf bank_mask:0xf
	v_mov_b32_dpp v115, v36 quad_perm:[1,0,3,2] row_mask:0xf bank_mask:0xf
	v_mov_b32_dpp v116, v20 quad_perm:[1,0,3,2] row_mask:0xf bank_mask:0xf
	v_mov_b32_dpp v117, v4 quad_perm:[1,0,3,2] row_mask:0xf bank_mask:0xf
	v_mov_b32_dpp v118, v53 quad_perm:[1,0,3,2] row_mask:0xf bank_mask:0xf
	v_mov_b32_dpp v119, v37 quad_perm:[1,0,3,2] row_mask:0xf bank_mask:0xf
	v_mov_b32_dpp v120, v21 quad_perm:[1,0,3,2] row_mask:0xf bank_mask:0xf
	v_mov_b32_dpp v121, v5 quad_perm:[1,0,3,2] row_mask:0xf bank_mask:0xf
	v_cvt_pk_bf16_f32 v52, v52, v114
	v_cvt_pk_bf16_f32 v36, v36, v115
	v_cvt_pk_bf16_f32 v20, v20, v116
	v_cvt_pk_bf16_f32 v4, v4, v117
	v_cvt_pk_bf16_f32 v53, v53, v118
	v_cvt_pk_bf16_f32 v37, v37, v119
	v_cvt_pk_bf16_f32 v21, v21, v120
	v_cvt_pk_bf16_f32 v5, v5, v121
	v_mul_f32_e32 v54, v54, v70
	v_mul_f32_e32 v38, v38, v70
	v_mul_f32_e32 v22, v22, v70
	v_mul_f32_e32 v6, v6, v70
	v_mul_f32_e32 v55, v55, v71
	v_mul_f32_e32 v39, v39, v71
	v_mul_f32_e32 v23, v23, v71
	v_mul_f32_e32 v7, v7, v71
	v_mov_b32_dpp v114, v54 quad_perm:[1,0,3,2] row_mask:0xf bank_mask:0xf
	v_mov_b32_dpp v115, v38 quad_perm:[1,0,3,2] row_mask:0xf bank_mask:0xf
	v_mov_b32_dpp v116, v22 quad_perm:[1,0,3,2] row_mask:0xf bank_mask:0xf
	v_mov_b32_dpp v117, v6 quad_perm:[1,0,3,2] row_mask:0xf bank_mask:0xf
	v_mov_b32_dpp v118, v55 quad_perm:[1,0,3,2] row_mask:0xf bank_mask:0xf
	v_mov_b32_dpp v119, v39 quad_perm:[1,0,3,2] row_mask:0xf bank_mask:0xf
	v_mov_b32_dpp v120, v23 quad_perm:[1,0,3,2] row_mask:0xf bank_mask:0xf
	v_mov_b32_dpp v121, v7 quad_perm:[1,0,3,2] row_mask:0xf bank_mask:0xf
	v_cvt_pk_bf16_f32 v54, v54, v114
	v_cvt_pk_bf16_f32 v38, v38, v115
	v_cvt_pk_bf16_f32 v22, v22, v116
	v_cvt_pk_bf16_f32 v6, v6, v117
	v_cvt_pk_bf16_f32 v55, v55, v118
	v_cvt_pk_bf16_f32 v39, v39, v119
	v_cvt_pk_bf16_f32 v23, v23, v120
	v_cvt_pk_bf16_f32 v7, v7, v121
	v_mul_f32_e32 v56, v56, v72
	v_mul_f32_e32 v40, v40, v72
	v_mul_f32_e32 v24, v24, v72
	v_mul_f32_e32 v8, v8, v72
	v_mul_f32_e32 v57, v57, v73
	v_mul_f32_e32 v41, v41, v73
	v_mul_f32_e32 v25, v25, v73
	v_mul_f32_e32 v9, v9, v73
	v_mov_b32_dpp v114, v56 quad_perm:[1,0,3,2] row_mask:0xf bank_mask:0xf
	v_mov_b32_dpp v115, v40 quad_perm:[1,0,3,2] row_mask:0xf bank_mask:0xf
	v_mov_b32_dpp v116, v24 quad_perm:[1,0,3,2] row_mask:0xf bank_mask:0xf
	v_mov_b32_dpp v117, v8 quad_perm:[1,0,3,2] row_mask:0xf bank_mask:0xf
	v_mov_b32_dpp v118, v57 quad_perm:[1,0,3,2] row_mask:0xf bank_mask:0xf
	v_mov_b32_dpp v119, v41 quad_perm:[1,0,3,2] row_mask:0xf bank_mask:0xf
	v_mov_b32_dpp v120, v25 quad_perm:[1,0,3,2] row_mask:0xf bank_mask:0xf
	v_mov_b32_dpp v121, v9 quad_perm:[1,0,3,2] row_mask:0xf bank_mask:0xf
	v_cvt_pk_bf16_f32 v56, v56, v114
	v_cvt_pk_bf16_f32 v40, v40, v115
	v_cvt_pk_bf16_f32 v24, v24, v116
	v_cvt_pk_bf16_f32 v8, v8, v117
	v_cvt_pk_bf16_f32 v57, v57, v118
	v_cvt_pk_bf16_f32 v41, v41, v119
	v_cvt_pk_bf16_f32 v25, v25, v120
	v_cvt_pk_bf16_f32 v9, v9, v121
	v_mul_f32_e32 v58, v58, v74
	v_mul_f32_e32 v42, v42, v74
	v_mul_f32_e32 v26, v26, v74
	v_mul_f32_e32 v10, v10, v74
	v_mul_f32_e32 v59, v59, v75
	v_mul_f32_e32 v43, v43, v75
	v_mul_f32_e32 v27, v27, v75
	v_mul_f32_e32 v11, v11, v75
	v_mov_b32_dpp v114, v58 quad_perm:[1,0,3,2] row_mask:0xf bank_mask:0xf
	v_mov_b32_dpp v115, v42 quad_perm:[1,0,3,2] row_mask:0xf bank_mask:0xf
	v_mov_b32_dpp v116, v26 quad_perm:[1,0,3,2] row_mask:0xf bank_mask:0xf
	v_mov_b32_dpp v117, v10 quad_perm:[1,0,3,2] row_mask:0xf bank_mask:0xf
	v_mov_b32_dpp v118, v59 quad_perm:[1,0,3,2] row_mask:0xf bank_mask:0xf
	v_mov_b32_dpp v119, v43 quad_perm:[1,0,3,2] row_mask:0xf bank_mask:0xf
	v_mov_b32_dpp v120, v27 quad_perm:[1,0,3,2] row_mask:0xf bank_mask:0xf
	v_mov_b32_dpp v121, v11 quad_perm:[1,0,3,2] row_mask:0xf bank_mask:0xf
	v_cvt_pk_bf16_f32 v58, v58, v114
	v_cvt_pk_bf16_f32 v42, v42, v115
	v_cvt_pk_bf16_f32 v26, v26, v116
	v_cvt_pk_bf16_f32 v10, v10, v117
	v_cvt_pk_bf16_f32 v59, v59, v118
	v_cvt_pk_bf16_f32 v43, v43, v119
	v_cvt_pk_bf16_f32 v27, v27, v120
	v_cvt_pk_bf16_f32 v11, v11, v121
	v_mul_f32_e32 v60, v60, v76
	v_mul_f32_e32 v44, v44, v76
	v_mul_f32_e32 v28, v28, v76
	v_mul_f32_e32 v12, v12, v76
	v_mul_f32_e32 v61, v61, v77
	v_mul_f32_e32 v45, v45, v77
	v_mul_f32_e32 v29, v29, v77
	v_mul_f32_e32 v13, v13, v77
	v_mov_b32_dpp v114, v60 quad_perm:[1,0,3,2] row_mask:0xf bank_mask:0xf
	v_mov_b32_dpp v115, v44 quad_perm:[1,0,3,2] row_mask:0xf bank_mask:0xf
	v_mov_b32_dpp v116, v28 quad_perm:[1,0,3,2] row_mask:0xf bank_mask:0xf
	v_mov_b32_dpp v117, v12 quad_perm:[1,0,3,2] row_mask:0xf bank_mask:0xf
	v_mov_b32_dpp v118, v61 quad_perm:[1,0,3,2] row_mask:0xf bank_mask:0xf
	v_mov_b32_dpp v119, v45 quad_perm:[1,0,3,2] row_mask:0xf bank_mask:0xf
	v_mov_b32_dpp v120, v29 quad_perm:[1,0,3,2] row_mask:0xf bank_mask:0xf
	v_mov_b32_dpp v121, v13 quad_perm:[1,0,3,2] row_mask:0xf bank_mask:0xf
	v_cvt_pk_bf16_f32 v60, v60, v114
	v_cvt_pk_bf16_f32 v44, v44, v115
	v_cvt_pk_bf16_f32 v28, v28, v116
	v_cvt_pk_bf16_f32 v12, v12, v117
	v_cvt_pk_bf16_f32 v61, v61, v118
	v_cvt_pk_bf16_f32 v45, v45, v119
	v_cvt_pk_bf16_f32 v29, v29, v120
	v_cvt_pk_bf16_f32 v13, v13, v121
	v_mul_f32_e32 v62, v62, v78
	v_mul_f32_e32 v46, v46, v78
	v_mul_f32_e32 v30, v30, v78
	v_mul_f32_e32 v14, v14, v78
	v_mul_f32_e32 v63, v63, v79
	v_mul_f32_e32 v47, v47, v79
	v_mul_f32_e32 v31, v31, v79
	v_mul_f32_e32 v15, v15, v79
	v_mov_b32_dpp v114, v62 quad_perm:[1,0,3,2] row_mask:0xf bank_mask:0xf
	v_mov_b32_dpp v115, v46 quad_perm:[1,0,3,2] row_mask:0xf bank_mask:0xf
	v_mov_b32_dpp v116, v30 quad_perm:[1,0,3,2] row_mask:0xf bank_mask:0xf
	v_mov_b32_dpp v117, v14 quad_perm:[1,0,3,2] row_mask:0xf bank_mask:0xf
	v_mov_b32_dpp v118, v63 quad_perm:[1,0,3,2] row_mask:0xf bank_mask:0xf
	v_mov_b32_dpp v119, v47 quad_perm:[1,0,3,2] row_mask:0xf bank_mask:0xf
	v_mov_b32_dpp v120, v31 quad_perm:[1,0,3,2] row_mask:0xf bank_mask:0xf
	v_mov_b32_dpp v121, v15 quad_perm:[1,0,3,2] row_mask:0xf bank_mask:0xf
	v_cvt_pk_bf16_f32 v62, v62, v114
	v_cvt_pk_bf16_f32 v46, v46, v115
	v_cvt_pk_bf16_f32 v30, v30, v116
	v_cvt_pk_bf16_f32 v14, v14, v117
	v_cvt_pk_bf16_f32 v63, v63, v118
	v_cvt_pk_bf16_f32 v47, v47, v119
	v_cvt_pk_bf16_f32 v31, v31, v120
	v_cvt_pk_bf16_f32 v15, v15, v121
	v_mul_f32_e32 v64, v64, v80
	v_mul_f32_e32 v48, v48, v80
	v_mul_f32_e32 v32, v32, v80
	v_mul_f32_e32 v16, v16, v80
	v_mul_f32_e32 v65, v65, v81
	v_mul_f32_e32 v49, v49, v81
	v_mul_f32_e32 v33, v33, v81
	v_mul_f32_e32 v17, v17, v81
	v_mov_b32_dpp v114, v64 quad_perm:[1,0,3,2] row_mask:0xf bank_mask:0xf
	v_mov_b32_dpp v115, v48 quad_perm:[1,0,3,2] row_mask:0xf bank_mask:0xf
	v_mov_b32_dpp v116, v32 quad_perm:[1,0,3,2] row_mask:0xf bank_mask:0xf
	v_mov_b32_dpp v117, v16 quad_perm:[1,0,3,2] row_mask:0xf bank_mask:0xf
	v_mov_b32_dpp v118, v65 quad_perm:[1,0,3,2] row_mask:0xf bank_mask:0xf
	v_mov_b32_dpp v119, v49 quad_perm:[1,0,3,2] row_mask:0xf bank_mask:0xf
	v_mov_b32_dpp v120, v33 quad_perm:[1,0,3,2] row_mask:0xf bank_mask:0xf
	v_mov_b32_dpp v121, v17 quad_perm:[1,0,3,2] row_mask:0xf bank_mask:0xf
	v_cvt_pk_bf16_f32 v64, v64, v114
	v_cvt_pk_bf16_f32 v48, v48, v115
	v_cvt_pk_bf16_f32 v32, v32, v116
	v_cvt_pk_bf16_f32 v16, v16, v117
	v_cvt_pk_bf16_f32 v65, v65, v118
	v_cvt_pk_bf16_f32 v49, v49, v119
	v_cvt_pk_bf16_f32 v33, v33, v120
	v_cvt_pk_bf16_f32 v17, v17, v121
	s_mov_b64 s[100:101], exec
	s_and_b64 exec, exec, s[6:7]
	ds_write_b32 v83, v50
	ds_write_b32 v83, v34 offset:64
	ds_write_b32 v83, v18 offset:128
	ds_write_b32 v83, v2 offset:192
	ds_write_b32 v83, v51 offset:256
	ds_write_b32 v83, v35 offset:320
	ds_write_b32 v83, v19 offset:384
	ds_write_b32 v83, v3 offset:448
	ds_write_b32 v83, v52 offset:512
	ds_write_b32 v83, v36 offset:576
	ds_write_b32 v83, v20 offset:640
	ds_write_b32 v83, v4 offset:704
	ds_write_b32 v83, v53 offset:768
	ds_write_b32 v83, v37 offset:832
	ds_write_b32 v83, v21 offset:896
	ds_write_b32 v83, v5 offset:960
	ds_write_b32 v83, v54 offset:2048
	ds_write_b32 v83, v38 offset:2112
	ds_write_b32 v83, v22 offset:2176
	ds_write_b32 v83, v6 offset:2240
	ds_write_b32 v83, v55 offset:2304
	ds_write_b32 v83, v39 offset:2368
	ds_write_b32 v83, v23 offset:2432
	ds_write_b32 v83, v7 offset:2496
	ds_write_b32 v83, v56 offset:2560
	ds_write_b32 v83, v40 offset:2624
	ds_write_b32 v83, v24 offset:2688
	ds_write_b32 v83, v8 offset:2752
	ds_write_b32 v83, v57 offset:2816
	ds_write_b32 v83, v41 offset:2880
	ds_write_b32 v83, v25 offset:2944
	ds_write_b32 v83, v9 offset:3008
	ds_write_b32 v83, v58 offset:4096
	ds_write_b32 v83, v42 offset:4160
	ds_write_b32 v83, v26 offset:4224
	ds_write_b32 v83, v10 offset:4288
	ds_write_b32 v83, v59 offset:4352
	ds_write_b32 v83, v43 offset:4416
	ds_write_b32 v83, v27 offset:4480
	ds_write_b32 v83, v11 offset:4544
	ds_write_b32 v83, v60 offset:4608
	ds_write_b32 v83, v44 offset:4672
	ds_write_b32 v83, v28 offset:4736
	ds_write_b32 v83, v12 offset:4800
	ds_write_b32 v83, v61 offset:4864
	ds_write_b32 v83, v45 offset:4928
	ds_write_b32 v83, v29 offset:4992
	ds_write_b32 v83, v13 offset:5056
	ds_write_b32 v83, v62 offset:6144
	ds_write_b32 v83, v46 offset:6208
	ds_write_b32 v83, v30 offset:6272
	ds_write_b32 v83, v14 offset:6336
	ds_write_b32 v83, v63 offset:6400
	ds_write_b32 v83, v47 offset:6464
	ds_write_b32 v83, v31 offset:6528
	ds_write_b32 v83, v15 offset:6592
	ds_write_b32 v83, v64 offset:6656
	ds_write_b32 v83, v48 offset:6720
	ds_write_b32 v83, v32 offset:6784
	ds_write_b32 v83, v16 offset:6848
	ds_write_b32 v83, v65 offset:6912
	ds_write_b32 v83, v49 offset:6976
	ds_write_b32 v83, v33 offset:7040
	ds_write_b32 v83, v17 offset:7104
	s_mov_b64 exec, s[100:101]
	ds_read_b128 v[66:69], v82
	ds_read_b128 v[70:73], v82 offset:1024
	ds_read_b128 v[74:77], v82 offset:2048
	ds_read_b128 v[78:81], v82 offset:3072
	ds_read_b128 v[86:89], v82 offset:4096
	ds_read_b128 v[90:93], v82 offset:5120
	ds_read_b128 v[94:97], v82 offset:6144
	ds_read_b128 v[98:101], v82 offset:7168
	s_waitcnt lgkmcnt(7)
	global_store_dwordx4 v84, v[66:69], s[0:1] nt
	s_waitcnt lgkmcnt(6)
	v_add_u32_e32 v85, 16384, v84
	global_store_dwordx4 v85, v[70:73], s[0:1] nt
	s_waitcnt lgkmcnt(5)
	v_add_u32_e32 v85, 32768, v84
	global_store_dwordx4 v85, v[74:77], s[0:1] nt
	s_waitcnt lgkmcnt(4)
	v_add_u32_e32 v85, 49152, v84
	global_store_dwordx4 v85, v[78:81], s[0:1] nt
	s_waitcnt lgkmcnt(3)
	v_add_u32_e32 v85, 65536, v84
	global_store_dwordx4 v85, v[86:89], s[0:1] nt
	s_waitcnt lgkmcnt(2)
	v_add_u32_e32 v85, 81920, v84
	global_store_dwordx4 v85, v[90:93], s[0:1] nt
	s_waitcnt lgkmcnt(1)
	v_add_u32_e32 v85, 98304, v84
	global_store_dwordx4 v85, v[94:97], s[0:1] nt
	s_waitcnt lgkmcnt(0)
	v_add_u32_e32 v85, 114688, v84
	global_store_dwordx4 v85, v[98:101], s[0:1] nt
	s_branch .LBB0_819
